# T10c seam fill NW7 with unequal shares: the 64 workgroups without an adaLN item convert 6 units per wave at seam 0 (they idle there) and own 133 units, the others 105 (one unit per wave per seam, no e
# speedup vs baseline: 1.0106x; 1.0027x over previous
; __device__ __forceinline__ void moe_convert(Frame& F, int lo, int hi, int rank, int nrank) {
;     if (MOE_DMA) { moe_convert_dma(F, lo, hi, rank, nrank); return; }
;     for (int it = lo + rank; it < hi; it += nrank) {
;         int r = it; const float* W; unsigned char* WT; int N, ldt, kind, off; float f8s;
;         if (r < 14336) { const int e = r / 1792; r -= e * 1792; W = F.in[IN_WMG] + (size_t)e * 2048 * DFFE; N = DFFE; WT = F.ws + WS_WGU1 + (size_t)e * 14336 * 2048; ldt = 2048; kind = 1; off = 0; f8s = 32.f; }
;         else if ((r -= 14336) < 14336) { const int e = r / 1792; r -= e * 1792; W = F.in[IN_WMU] + (size_t)e * 2048 * DFFE; N = DFFE; WT = F.ws + WS_WGU1 + (size_t)e * 14336 * 2048; ldt = 2048; kind = 1; off = 128; f8s = 256.f; }
;         else { r -= 14336; const int e = r / 1792; r -= e * 1792; W = F.in[IN_WMD] + (size_t)e * DFFE * 2048; N = 2048; WT = F.ws + WS_WDN1 + (size_t)e * 2048 * DFFE; ldt = DFFE; kind = 0; off = 0; f8s = 64.f; }
;         transpose_item_f8(W, N, WT, ldt, kind, off, r, F.lane, f8s);
;     }
.Lsf0_notw0:
	s_cmp_gt_u32 s4, 7
	s_cbranch_scc1 .Lsf0_skip
	v_mov_b32_e32 v8, 0x20020
	ds_read_b32 v9, v8 offset:4
	v_mbcnt_lo_u32_b32 v2, -1, 0
	v_mbcnt_hi_u32_b32 v2, -1, v2
	v_readlane_b32 s39, v247, 6
	s_movk_i32 s40, 105
	s_and_b32 s41, s39, 7
	s_cmp_ge_u32 s41, 6
	s_cselect_b32 s40, 133, s40
	s_cselect_b32 s34, 6, 1
	s_waitcnt lgkmcnt(0)
	v_readfirstlane_b32 s5, v9
	s_cmp_ge_u32 s5, s40
	s_cbranch_scc1 .Lsf0_skip
	s_add_i32 s5, s4, -1
	s_lshl_b32 s5, s5, 14
	v_lshl_add_u32 v7, v2, 4, s5
	ds_write_b128 v7, v[160:163] offset:0
	ds_write_b128 v7, v[164:167] offset:1024
	ds_write_b128 v7, v[168:171] offset:2048
	ds_write_b128 v7, v[172:175] offset:3072
	ds_write_b128 v7, v[176:179] offset:4096
	ds_write_b128 v7, v[180:183] offset:5120
	ds_write_b128 v7, v[184:187] offset:6144
	ds_write_b128 v7, v[188:191] offset:7168
	ds_write_b128 v7, v[192:195] offset:8192
	ds_write_b128 v7, v[196:199] offset:9216
	ds_write_b128 v7, v[200:203] offset:10240
	ds_write_b128 v7, v[204:207] offset:11264
	ds_write_b128 v7, v[208:211] offset:12288
	ds_write_b128 v7, v[212:215] offset:13312
	ds_write_b128 v7, v[216:219] offset:14336
	ds_write_b128 v7, v[220:223] offset:15360
	v_readlane_b32 s6, v247, 0
	v_readlane_b32 s7, v247, 1
	s_load_dwordx2 s[10:11], s[6:7], 0xc0
	s_load_dwordx2 s[12:13], s[6:7], 0xc8
	v_mov_b32_e32 v3, 0x43e00000
	v_cmp_eq_u32_e32 vcc, 0, v2
	s_lshr_b32 s42, s39, 3
	s_mul_i32 s42, s42, 896
	s_min_u32 s43, s41, 6
	s_mul_i32 s43, s43, 105
	s_max_u32 s44, s41, 6
	s_sub_u32 s44, s44, 6
	s_mul_i32 s44, s44, 133
	s_add_i32 s33, s42, s43
	s_add_i32 s33, s33, s44
	v_cndmask_b32_e64 v18, 0, 1, vcc
	s_waitcnt lgkmcnt(0)
.Lsf0_loop:
	ds_add_rtn_u32 v9, v8, v18 offset:4
	s_waitcnt lgkmcnt(0)
	v_readfirstlane_b32 s18, v9
	s_cmp_ge_u32 s18, s40
	s_cbranch_scc1 .Lsf0_done
	s_add_i32 s18, s18, s33
	s_and_b32 s27, s18, 1
	s_lshr_b32 s19, s18, 1
	s_add_i32 s19, s19, 0x5000
	s_cmp_lt_u32 s19, 0x7000
	s_cbranch_scc0 .Lsf0_down
	s_add_i32 s20, s19, 0xffffc800
	s_lshr_b32 s21, s20, 8
	s_mul_i32 s21, s21, 37
	s_lshr_b32 s21, s21, 8
	s_mul_i32 s28, s21, 0x700
	s_sub_i32 s20, s20, s28
	s_mul_i32 s28, s21, 0x3800000
	s_add_u32 s14, s10, s28
	s_addc_u32 s15, s11, 0
	s_mul_i32 s28, s21, 0x1c00000
	s_add_u32 s28, s28, 0x7800000
	s_add_u32 s16, s86, s28
	s_addc_u32 s17, s87, 0
	s_movk_i32 s24, 0x7000
	s_movk_i32 s25, 0x800
	s_mov_b32 s26, 0x43800000
	s_lshr_b32 s22, s20, 4
	s_mul_i32 s22, s22, 0x2493
	s_lshr_b32 s22, s22, 16
	s_mul_i32 s28, s22, 0x70
	s_sub_i32 s23, s20, s28
	s_mov_b32 s29, 1
	s_branch .Lsf0_dec

; __device__ __forceinline__ void moe_convert(Frame& F, int lo, int hi, int rank, int nrank) {
;     if (MOE_DMA) { moe_convert_dma(F, lo, hi, rank, nrank); return; }
;     for (int it = lo + rank; it < hi; it += nrank) {
;         int r = it; const float* W; unsigned char* WT; int N, ldt, kind, off; float f8s;
;         if (r < 14336) { const int e = r / 1792; r -= e * 1792; W = F.in[IN_WMG] + (size_t)e * 2048 * DFFE; N = DFFE; WT = F.ws + WS_WGU1 + (size_t)e * 14336 * 2048; ldt = 2048; kind = 1; off = 0; f8s = 32.f; }
;         else if ((r -= 14336) < 14336) { const int e = r / 1792; r -= e * 1792; W = F.in[IN_WMU] + (size_t)e * 2048 * DFFE; N = DFFE; WT = F.ws + WS_WGU1 + (size_t)e * 14336 * 2048; ldt = 2048; kind = 1; off = 128; f8s = 256.f; }
;         else { r -= 14336; const int e = r / 1792; r -= e * 1792; W = F.in[IN_WMD] + (size_t)e * DFFE * 2048; N = 2048; WT = F.ws + WS_WDN1 + (size_t)e * 2048 * DFFE; ldt = DFFE; kind = 0; off = 0; f8s = 64.f; }
;         transpose_item_f8(W, N, WT, ldt, kind, off, r, F.lane, f8s);
;     }
.Lsf1_notw0:
	s_cmp_gt_u32 s4, 7
	s_cbranch_scc1 .Lsf1_skip
	v_mov_b32_e32 v8, 0x20020
	ds_read_b32 v9, v8 offset:4
	v_mbcnt_lo_u32_b32 v2, -1, 0
	v_mbcnt_hi_u32_b32 v2, -1, v2
	v_readlane_b32 s39, v247, 6
	s_movk_i32 s40, 105
	s_and_b32 s41, s39, 7
	s_cmp_ge_u32 s41, 6
	s_cselect_b32 s40, 133, s40
	s_waitcnt lgkmcnt(0)
	v_readfirstlane_b32 s5, v9
	s_cmp_ge_u32 s5, s40
	s_cbranch_scc1 .Lsf1_skip
	s_add_i32 s5, s4, -1
	s_lshl_b32 s5, s5, 14
	v_lshl_add_u32 v7, v2, 4, s5
	ds_write_b128 v7, v[160:163] offset:0
	ds_write_b128 v7, v[164:167] offset:1024
	ds_write_b128 v7, v[168:171] offset:2048
	ds_write_b128 v7, v[172:175] offset:3072
	ds_write_b128 v7, v[176:179] offset:4096
	ds_write_b128 v7, v[180:183] offset:5120
	ds_write_b128 v7, v[184:187] offset:6144
	ds_write_b128 v7, v[188:191] offset:7168
	ds_write_b128 v7, v[192:195] offset:8192
	ds_write_b128 v7, v[196:199] offset:9216
	ds_write_b128 v7, v[200:203] offset:10240
	ds_write_b128 v7, v[204:207] offset:11264
	ds_write_b128 v7, v[208:211] offset:12288
	ds_write_b128 v7, v[212:215] offset:13312
	ds_write_b128 v7, v[216:219] offset:14336
	ds_write_b128 v7, v[220:223] offset:15360
	v_readlane_b32 s6, v247, 0
	v_readlane_b32 s7, v247, 1
	s_load_dwordx2 s[10:11], s[6:7], 0xc0
	s_load_dwordx2 s[12:13], s[6:7], 0xc8
	v_mov_b32_e32 v3, 0x43e00000
	v_cmp_eq_u32_e32 vcc, 0, v2
	s_lshr_b32 s42, s39, 3
	s_mul_i32 s42, s42, 896
	s_min_u32 s43, s41, 6
	s_mul_i32 s43, s43, 105
	s_max_u32 s44, s41, 6
	s_sub_u32 s44, s44, 6
	s_mul_i32 s44, s44, 133
	s_add_i32 s33, s42, s43
	s_add_i32 s33, s33, s44
	v_cndmask_b32_e64 v18, 0, 1, vcc
	s_waitcnt lgkmcnt(0)
	s_mov_b32 s34, 1
.Lsf1_loop:
	ds_read_b32 v9, v8
	s_waitcnt lgkmcnt(0)
	v_readfirstlane_b32 s5, v9
	s_cmp_eq_u32 s5, 2
	s_cbranch_scc1 .Lsf1_done
	ds_add_rtn_u32 v9, v8, v18 offset:4
	s_waitcnt lgkmcnt(0)
	v_readfirstlane_b32 s18, v9
	s_cmp_ge_u32 s18, s40
	s_cbranch_scc1 .Lsf1_done
	s_add_i32 s18, s18, s33
	s_and_b32 s27, s18, 1
	s_lshr_b32 s19, s18, 1
	s_add_i32 s19, s19, 0x5000
	s_cmp_lt_u32 s19, 0x7000
	s_cbranch_scc0 .Lsf1_down
	s_add_i32 s20, s19, 0xffffc800
	s_lshr_b32 s21, s20, 8
	s_mul_i32 s21, s21, 37
	s_lshr_b32 s21, s21, 8
	s_mul_i32 s28, s21, 0x700
	s_sub_i32 s20, s20, s28
	s_mul_i32 s28, s21, 0x3800000
	s_add_u32 s14, s10, s28
	s_addc_u32 s15, s11, 0
	s_mul_i32 s28, s21, 0x1c00000
	s_add_u32 s28, s28, 0x7800000
	s_add_u32 s16, s86, s28
	s_addc_u32 s17, s87, 0
	s_movk_i32 s24, 0x7000
	s_movk_i32 s25, 0x800
	s_mov_b32 s26, 0x43800000
	s_lshr_b32 s22, s20, 4
	s_mul_i32 s22, s22, 0x2493
	s_lshr_b32 s22, s22, 16
	s_mul_i32 s28, s22, 0x70
	s_sub_i32 s23, s20, s28
	s_mov_b32 s29, 1
	s_branch .Lsf1_dec

; __device__ __forceinline__ void transpose_item_f8(const float* W, int N, unsigned char* WT, int ldt, int kind, int off, int item, int lane, float scale) {
;     const int nblk = N >> 6, kb = item / nblk, nb = item - kb * nblk, k0 = 128 * kb + 16 * (lane & 7), n = 64 * nb + 4 * (lane >> 3);
; __device__ __forceinline__ void moe_convert(Frame& F, int lo, int hi, int rank, int nrank) {
;     ...
;     for (int it = lo + rank; it < hi; it += nrank) {
;         int r = it; const float* W; unsigned char* WT; int N, ldt, kind, off; float f8s;
;         if (r < 14336) { const int e = r / 1792; r -= e * 1792; W = F.in[IN_WMG] + (size_t)e * 2048 * DFFE; N = DFFE; WT = F.ws + WS_WGU1 + (size_t)e * 14336 * 2048; ldt = 2048; kind = 1; off = 0; f8s = 32.f; }
;         else if ((r -= 14336) < 14336) { const int e = r / 1792; r -= e * 1792; W = F.in[IN_WMU] + (size_t)e * 2048 * DFFE; N = DFFE; WT = F.ws + WS_WGU1 + (size_t)e * 14336 * 2048; ldt = 2048; kind = 1; off = 128; f8s = 256.f; }
;         else { r -= 14336; const int e = r / 1792; r -= e * 1792; W = F.in[IN_WMD] + (size_t)e * DFFE * 2048; N = 2048; WT = F.ws + WS_WDN1 + (size_t)e * 2048 * DFFE; ldt = DFFE; kind = 0; off = 0; f8s = 64.f; }
;         transpose_item_f8(W, N, WT, ldt, kind, off, r, F.lane, f8s);
.Lsf2_loop:
	ds_read_b32 v9, v8
	s_waitcnt lgkmcnt(0)
	v_readfirstlane_b32 s5, v9
	s_cmp_eq_u32 s5, 3
	s_cbranch_scc1 .Lsf2_done
	ds_add_rtn_u32 v9, v8, v18 offset:4
	s_waitcnt lgkmcnt(0)
	v_readfirstlane_b32 s18, v9
	s_cmp_ge_u32 s18, s40
	s_cbranch_scc1 .Lsf2_done
	s_add_i32 s18, s18, s33
	s_and_b32 s27, s18, 1
	s_lshr_b32 s19, s18, 1
	s_add_i32 s19, s19, 0x5000
	s_cmp_lt_u32 s19, 0x7000
	s_cbranch_scc0 .Lsf2_down
	s_add_i32 s20, s19, 0xffffc800
	s_lshr_b32 s21, s20, 8
	s_mul_i32 s21, s21, 37
	s_lshr_b32 s21, s21, 8
	s_mul_i32 s28, s21, 0x700
	s_sub_i32 s20, s20, s28
	s_mul_i32 s28, s21, 0x3800000
	s_add_u32 s14, s10, s28
	s_addc_u32 s15, s11, 0
	s_mul_i32 s28, s21, 0x1c00000
	s_add_u32 s28, s28, 0x7800000
	s_add_u32 s16, s86, s28
	s_addc_u32 s17, s87, 0
	s_movk_i32 s24, 0x7000
	s_movk_i32 s25, 0x800
	s_mov_b32 s26, 0x43800000
	s_lshr_b32 s22, s20, 4
	s_mul_i32 s22, s22, 0x2493
	s_lshr_b32 s22, s22, 16
	s_mul_i32 s28, s22, 0x70
	s_sub_i32 s23, s20, s28
	s_mov_b32 s29, 1
	s_branch .Lsf2_dec

; __device__ __forceinline__ void transpose_item_f8(const float* W, int N, unsigned char* WT, int ldt, int kind, int off, int item, int lane, float scale) {
;     const int nblk = N >> 6, kb = item / nblk, nb = item - kb * nblk, k0 = 128 * kb + 16 * (lane & 7), n = 64 * nb + 4 * (lane >> 3);
; __device__ __forceinline__ void moe_convert(Frame& F, int lo, int hi, int rank, int nrank) {
;     ...
;     for (int it = lo + rank; it < hi; it += nrank) {
;         int r = it; const float* W; unsigned char* WT; int N, ldt, kind, off; float f8s;
;         if (r < 14336) { const int e = r / 1792; r -= e * 1792; W = F.in[IN_WMG] + (size_t)e * 2048 * DFFE; N = DFFE; WT = F.ws + WS_WGU1 + (size_t)e * 14336 * 2048; ldt = 2048; kind = 1; off = 0; f8s = 32.f; }
;         else if ((r -= 14336) < 14336) { const int e = r / 1792; r -= e * 1792; W = F.in[IN_WMU] + (size_t)e * 2048 * DFFE; N = DFFE; WT = F.ws + WS_WGU1 + (size_t)e * 14336 * 2048; ldt = 2048; kind = 1; off = 128; f8s = 256.f; }
;         else { r -= 14336; const int e = r / 1792; r -= e * 1792; W = F.in[IN_WMD] + (size_t)e * DFFE * 2048; N = 2048; WT = F.ws + WS_WDN1 + (size_t)e * 2048 * DFFE; ldt = DFFE; kind = 0; off = 0; f8s = 64.f; }
;         transpose_item_f8(W, N, WT, ldt, kind, off, r, F.lane, f8s);
.Lsf3_loop:
	ds_read_b32 v9, v8
	s_waitcnt lgkmcnt(0)
	v_readfirstlane_b32 s5, v9
	s_cmp_eq_u32 s5, 4
	s_cbranch_scc1 .Lsf3_done
	ds_add_rtn_u32 v9, v8, v18 offset:4
	s_waitcnt lgkmcnt(0)
	v_readfirstlane_b32 s18, v9
	s_cmp_ge_u32 s18, s40
	s_cbranch_scc1 .Lsf3_done
	s_add_i32 s18, s18, s33
	s_and_b32 s27, s18, 1
	s_lshr_b32 s19, s18, 1
	s_add_i32 s19, s19, 0x5000
	s_cmp_lt_u32 s19, 0x7000
	s_cbranch_scc0 .Lsf3_down
	s_add_i32 s20, s19, 0xffffc800
	s_lshr_b32 s21, s20, 8
	s_mul_i32 s21, s21, 37
	s_lshr_b32 s21, s21, 8
	s_mul_i32 s28, s21, 0x700
	s_sub_i32 s20, s20, s28
	s_mul_i32 s28, s21, 0x3800000
	s_add_u32 s14, s10, s28
	s_addc_u32 s15, s11, 0
	s_mul_i32 s28, s21, 0x1c00000
	s_add_u32 s28, s28, 0x7800000
	s_add_u32 s16, s86, s28
	s_addc_u32 s17, s87, 0
	s_movk_i32 s24, 0x7000
	s_movk_i32 s25, 0x800
	s_mov_b32 s26, 0x43800000
	s_lshr_b32 s22, s20, 4
	s_mul_i32 s22, s22, 0x2493
	s_lshr_b32 s22, s22, 16
	s_mul_i32 s28, s22, 0x70
	s_sub_i32 s23, s20, s28
	s_mov_b32 s29, 1
	s_branch .Lsf3_dec

; __device__ __forceinline__ void transpose_item_f8(const float* W, int N, unsigned char* WT, int ldt, int kind, int off, int item, int lane, float scale) {
;     const int nblk = N >> 6, kb = item / nblk, nb = item - kb * nblk, k0 = 128 * kb + 16 * (lane & 7), n = 64 * nb + 4 * (lane >> 3);
; __device__ __forceinline__ void moe_convert(Frame& F, int lo, int hi, int rank, int nrank) {
;     ...
;     for (int it = lo + rank; it < hi; it += nrank) {
;         int r = it; const float* W; unsigned char* WT; int N, ldt, kind, off; float f8s;
;         if (r < 14336) { const int e = r / 1792; r -= e * 1792; W = F.in[IN_WMG] + (size_t)e * 2048 * DFFE; N = DFFE; WT = F.ws + WS_WGU1 + (size_t)e * 14336 * 2048; ldt = 2048; kind = 1; off = 0; f8s = 32.f; }
;         else if ((r -= 14336) < 14336) { const int e = r / 1792; r -= e * 1792; W = F.in[IN_WMU] + (size_t)e * 2048 * DFFE; N = DFFE; WT = F.ws + WS_WGU1 + (size_t)e * 14336 * 2048; ldt = 2048; kind = 1; off = 128; f8s = 256.f; }
;         else { r -= 14336; const int e = r / 1792; r -= e * 1792; W = F.in[IN_WMD] + (size_t)e * DFFE * 2048; N = 2048; WT = F.ws + WS_WDN1 + (size_t)e * 2048 * DFFE; ldt = DFFE; kind = 0; off = 0; f8s = 64.f; }
;         transpose_item_f8(W, N, WT, ldt, kind, off, r, F.lane, f8s);
.Lsf4_loop:
	ds_read_b32 v9, v8
	s_waitcnt lgkmcnt(0)
	v_readfirstlane_b32 s5, v9
	s_cmp_eq_u32 s5, 5
	s_cbranch_scc1 .Lsf4_done
	ds_add_rtn_u32 v9, v8, v18 offset:4
	s_waitcnt lgkmcnt(0)
	v_readfirstlane_b32 s18, v9
	s_cmp_ge_u32 s18, s40
	s_cbranch_scc1 .Lsf4_done
	s_add_i32 s18, s18, s33
	s_and_b32 s27, s18, 1
	s_lshr_b32 s19, s18, 1
	s_add_i32 s19, s19, 0x5000
	s_cmp_lt_u32 s19, 0x7000
	s_cbranch_scc0 .Lsf4_down
	s_add_i32 s20, s19, 0xffffc800
	s_lshr_b32 s21, s20, 8
	s_mul_i32 s21, s21, 37
	s_lshr_b32 s21, s21, 8
	s_mul_i32 s28, s21, 0x700
	s_sub_i32 s20, s20, s28
	s_mul_i32 s28, s21, 0x3800000
	s_add_u32 s14, s10, s28
	s_addc_u32 s15, s11, 0
	s_mul_i32 s28, s21, 0x1c00000
	s_add_u32 s28, s28, 0x7800000
	s_add_u32 s16, s86, s28
	s_addc_u32 s17, s87, 0
	s_movk_i32 s24, 0x7000
	s_movk_i32 s25, 0x800
	s_mov_b32 s26, 0x43800000
	s_lshr_b32 s22, s20, 4
	s_mul_i32 s22, s22, 0x2493
	s_lshr_b32 s22, s22, 16
	s_mul_i32 s28, s22, 0x70
	s_sub_i32 s23, s20, s28
	s_mov_b32 s29, 1
	s_branch .Lsf4_dec

; __device__ __forceinline__ void transpose_item_f8(const float* W, int N, unsigned char* WT, int ldt, int kind, int off, int item, int lane, float scale) {
;     const int nblk = N >> 6, kb = item / nblk, nb = item - kb * nblk, k0 = 128 * kb + 16 * (lane & 7), n = 64 * nb + 4 * (lane >> 3);
; __device__ __forceinline__ void moe_convert(Frame& F, int lo, int hi, int rank, int nrank) {
;     ...
;     for (int it = lo + rank; it < hi; it += nrank) {
;         int r = it; const float* W; unsigned char* WT; int N, ldt, kind, off; float f8s;
;         if (r < 14336) { const int e = r / 1792; r -= e * 1792; W = F.in[IN_WMG] + (size_t)e * 2048 * DFFE; N = DFFE; WT = F.ws + WS_WGU1 + (size_t)e * 14336 * 2048; ldt = 2048; kind = 1; off = 0; f8s = 32.f; }
;         else if ((r -= 14336) < 14336) { const int e = r / 1792; r -= e * 1792; W = F.in[IN_WMU] + (size_t)e * 2048 * DFFE; N = DFFE; WT = F.ws + WS_WGU1 + (size_t)e * 14336 * 2048; ldt = 2048; kind = 1; off = 128; f8s = 256.f; }
;         else { r -= 14336; const int e = r / 1792; r -= e * 1792; W = F.in[IN_WMD] + (size_t)e * DFFE * 2048; N = 2048; WT = F.ws + WS_WDN1 + (size_t)e * 2048 * DFFE; ldt = DFFE; kind = 0; off = 0; f8s = 64.f; }
;         transpose_item_f8(W, N, WT, ldt, kind, off, r, F.lane, f8s);
.Lsf5_loop:
	ds_read_b32 v9, v8
	s_waitcnt lgkmcnt(0)
	v_readfirstlane_b32 s5, v9
	s_cmp_eq_u32 s5, 6
	s_cbranch_scc1 .Lsf5_done
	ds_add_rtn_u32 v9, v8, v18 offset:4
	s_waitcnt lgkmcnt(0)
	v_readfirstlane_b32 s18, v9
	s_cmp_ge_u32 s18, s40
	s_cbranch_scc1 .Lsf5_done
	s_add_i32 s18, s18, s33
	s_and_b32 s27, s18, 1
	s_lshr_b32 s19, s18, 1
	s_add_i32 s19, s19, 0x5000
	s_cmp_lt_u32 s19, 0x7000
	s_cbranch_scc0 .Lsf5_down
	s_add_i32 s20, s19, 0xffffc800
	s_lshr_b32 s21, s20, 8
	s_mul_i32 s21, s21, 37
	s_lshr_b32 s21, s21, 8
	s_mul_i32 s28, s21, 0x700
	s_sub_i32 s20, s20, s28
	s_mul_i32 s28, s21, 0x3800000
	s_add_u32 s14, s10, s28
	s_addc_u32 s15, s11, 0
	s_mul_i32 s28, s21, 0x1c00000
	s_add_u32 s28, s28, 0x7800000
	s_add_u32 s16, s86, s28
	s_addc_u32 s17, s87, 0
	s_movk_i32 s24, 0x7000
	s_movk_i32 s25, 0x800
	s_mov_b32 s26, 0x43800000
	s_lshr_b32 s22, s20, 4
	s_mul_i32 s22, s22, 0x2493
	s_lshr_b32 s22, s22, 16
	s_mul_i32 s28, s22, 0x70
	s_sub_i32 s23, s20, s28
	s_mov_b32 s29, 1
	s_branch .Lsf5_dec

; __device__ __forceinline__ void transpose_item_f8(const float* W, int N, unsigned char* WT, int ldt, int kind, int off, int item, int lane, float scale) {
;     const int nblk = N >> 6, kb = item / nblk, nb = item - kb * nblk, k0 = 128 * kb + 16 * (lane & 7), n = 64 * nb + 4 * (lane >> 3);
; __device__ __forceinline__ void moe_convert(Frame& F, int lo, int hi, int rank, int nrank) {
;     ...
;     for (int it = lo + rank; it < hi; it += nrank) {
;         int r = it; const float* W; unsigned char* WT; int N, ldt, kind, off; float f8s;
;         if (r < 14336) { const int e = r / 1792; r -= e * 1792; W = F.in[IN_WMG] + (size_t)e * 2048 * DFFE; N = DFFE; WT = F.ws + WS_WGU1 + (size_t)e * 14336 * 2048; ldt = 2048; kind = 1; off = 0; f8s = 32.f; }
;         else if ((r -= 14336) < 14336) { const int e = r / 1792; r -= e * 1792; W = F.in[IN_WMU] + (size_t)e * 2048 * DFFE; N = DFFE; WT = F.ws + WS_WGU1 + (size_t)e * 14336 * 2048; ldt = 2048; kind = 1; off = 128; f8s = 256.f; }
;         else { r -= 14336; const int e = r / 1792; r -= e * 1792; W = F.in[IN_WMD] + (size_t)e * DFFE * 2048; N = 2048; WT = F.ws + WS_WDN1 + (size_t)e * 2048 * DFFE; ldt = DFFE; kind = 0; off = 0; f8s = 64.f; }
;         transpose_item_f8(W, N, WT, ldt, kind, off, r, F.lane, f8s);
.Lsf6_loop:
	ds_read_b32 v9, v8
	s_waitcnt lgkmcnt(0)
	v_readfirstlane_b32 s5, v9
	s_cmp_eq_u32 s5, 7
	s_cbranch_scc1 .Lsf6_done
	ds_add_rtn_u32 v9, v8, v18 offset:4
	s_waitcnt lgkmcnt(0)
	v_readfirstlane_b32 s18, v9
	s_cmp_ge_u32 s18, s40
	s_cbranch_scc1 .Lsf6_done
	s_add_i32 s18, s18, s33
	s_and_b32 s27, s18, 1
	s_lshr_b32 s19, s18, 1
	s_add_i32 s19, s19, 0x5000
	s_cmp_lt_u32 s19, 0x7000
	s_cbranch_scc0 .Lsf6_down
	s_add_i32 s20, s19, 0xffffc800
	s_lshr_b32 s21, s20, 8
	s_mul_i32 s21, s21, 37
	s_lshr_b32 s21, s21, 8
	s_mul_i32 s28, s21, 0x700
	s_sub_i32 s20, s20, s28
	s_mul_i32 s28, s21, 0x3800000
	s_add_u32 s14, s10, s28
	s_addc_u32 s15, s11, 0
	s_mul_i32 s28, s21, 0x1c00000
	s_add_u32 s28, s28, 0x7800000
	s_add_u32 s16, s86, s28
	s_addc_u32 s17, s87, 0
	s_movk_i32 s24, 0x7000
	s_movk_i32 s25, 0x800
	s_mov_b32 s26, 0x43800000
	s_lshr_b32 s22, s20, 4
	s_mul_i32 s22, s22, 0x2493
	s_lshr_b32 s22, s22, 16
	s_mul_i32 s28, s22, 0x70
	s_sub_i32 s23, s20, s28
	s_mov_b32 s29, 1
	s_branch .Lsf6_dec

; __device__ __forceinline__ void transpose_item_f8(const float* W, int N, unsigned char* WT, int ldt, int kind, int off, int item, int lane, float scale) {
;     const int nblk = N >> 6, kb = item / nblk, nb = item - kb * nblk, k0 = 128 * kb + 16 * (lane & 7), n = 64 * nb + 4 * (lane >> 3);
; __device__ __forceinline__ void moe_convert(Frame& F, int lo, int hi, int rank, int nrank) {
;     ...
;     for (int it = lo + rank; it < hi; it += nrank) {
;         int r = it; const float* W; unsigned char* WT; int N, ldt, kind, off; float f8s;
;         if (r < 14336) { const int e = r / 1792; r -= e * 1792; W = F.in[IN_WMG] + (size_t)e * 2048 * DFFE; N = DFFE; WT = F.ws + WS_WGU1 + (size_t)e * 14336 * 2048; ldt = 2048; kind = 1; off = 0; f8s = 32.f; }
;         else if ((r -= 14336) < 14336) { const int e = r / 1792; r -= e * 1792; W = F.in[IN_WMU] + (size_t)e * 2048 * DFFE; N = DFFE; WT = F.ws + WS_WGU1 + (size_t)e * 14336 * 2048; ldt = 2048; kind = 1; off = 128; f8s = 256.f; }
;         else { r -= 14336; const int e = r / 1792; r -= e * 1792; W = F.in[IN_WMD] + (size_t)e * DFFE * 2048; N = 2048; WT = F.ws + WS_WDN1 + (size_t)e * 2048 * DFFE; ldt = DFFE; kind = 0; off = 0; f8s = 64.f; }
;         transpose_item_f8(W, N, WT, ldt, kind, off, r, F.lane, f8s);
.Lsf7_loop:
	ds_read_b32 v9, v8
	s_waitcnt lgkmcnt(0)
	v_readfirstlane_b32 s5, v9
	s_cmp_eq_u32 s5, 8
	s_cbranch_scc1 .Lsf7_done
	ds_add_rtn_u32 v9, v8, v18 offset:4
	s_waitcnt lgkmcnt(0)
	v_readfirstlane_b32 s18, v9
	s_cmp_ge_u32 s18, s40
	s_cbranch_scc1 .Lsf7_done
	s_add_i32 s18, s18, s33
	s_and_b32 s27, s18, 1
	s_lshr_b32 s19, s18, 1
	s_add_i32 s19, s19, 0x5000
	s_cmp_lt_u32 s19, 0x7000
	s_cbranch_scc0 .Lsf7_down
	s_add_i32 s20, s19, 0xffffc800
	s_lshr_b32 s21, s20, 8
	s_mul_i32 s21, s21, 37
	s_lshr_b32 s21, s21, 8
	s_mul_i32 s28, s21, 0x700
	s_sub_i32 s20, s20, s28
	s_mul_i32 s28, s21, 0x3800000
	s_add_u32 s14, s10, s28
	s_addc_u32 s15, s11, 0
	s_mul_i32 s28, s21, 0x1c00000
	s_add_u32 s28, s28, 0x7800000
	s_add_u32 s16, s86, s28
	s_addc_u32 s17, s87, 0
	s_movk_i32 s24, 0x7000
	s_movk_i32 s25, 0x800
	s_mov_b32 s26, 0x43800000
	s_lshr_b32 s22, s20, 4
	s_mul_i32 s22, s22, 0x2493
	s_lshr_b32 s22, s22, 16
	s_mul_i32 s28, s22, 0x70
	s_sub_i32 s23, s20, s28
	s_mov_b32 s29, 1
	s_branch .Lsf7_dec

; __device__ __forceinline__ void transpose_item_f8(const float* W, int N, unsigned char* WT, int ldt, int kind, int off, int item, int lane, float scale) {
;     const int nblk = N >> 6, kb = item / nblk, nb = item - kb * nblk, k0 = 128 * kb + 16 * (lane & 7), n = 64 * nb + 4 * (lane >> 3);
; __device__ __forceinline__ void moe_convert(Frame& F, int lo, int hi, int rank, int nrank) {
;     ...
;     for (int it = lo + rank; it < hi; it += nrank) {
;         int r = it; const float* W; unsigned char* WT; int N, ldt, kind, off; float f8s;
;         if (r < 14336) { const int e = r / 1792; r -= e * 1792; W = F.in[IN_WMG] + (size_t)e * 2048 * DFFE; N = DFFE; WT = F.ws + WS_WGU1 + (size_t)e * 14336 * 2048; ldt = 2048; kind = 1; off = 0; f8s = 32.f; }
;         else if ((r -= 14336) < 14336) { const int e = r / 1792; r -= e * 1792; W = F.in[IN_WMU] + (size_t)e * 2048 * DFFE; N = DFFE; WT = F.ws + WS_WGU1 + (size_t)e * 14336 * 2048; ldt = 2048; kind = 1; off = 128; f8s = 256.f; }
;         else { r -= 14336; const int e = r / 1792; r -= e * 1792; W = F.in[IN_WMD] + (size_t)e * DFFE * 2048; N = 2048; WT = F.ws + WS_WDN1 + (size_t)e * 2048 * DFFE; ldt = DFFE; kind = 0; off = 0; f8s = 64.f; }
;         transpose_item_f8(W, N, WT, ldt, kind, off, r, F.lane, f8s);
.Lsf8_loop:
	ds_read_b32 v9, v8
	s_waitcnt lgkmcnt(0)
	v_readfirstlane_b32 s5, v9
	s_cmp_eq_u32 s5, 9
	s_cbranch_scc1 .Lsf8_done
	ds_add_rtn_u32 v9, v8, v18 offset:4
	s_waitcnt lgkmcnt(0)
	v_readfirstlane_b32 s18, v9
	s_cmp_ge_u32 s18, s40
	s_cbranch_scc1 .Lsf8_done
	s_add_i32 s18, s18, s33
	s_and_b32 s27, s18, 1
	s_lshr_b32 s19, s18, 1
	s_add_i32 s19, s19, 0x5000
	s_cmp_lt_u32 s19, 0x7000
	s_cbranch_scc0 .Lsf8_down
	s_add_i32 s20, s19, 0xffffc800
	s_lshr_b32 s21, s20, 8
	s_mul_i32 s21, s21, 37
	s_lshr_b32 s21, s21, 8
	s_mul_i32 s28, s21, 0x700
	s_sub_i32 s20, s20, s28
	s_mul_i32 s28, s21, 0x3800000
	s_add_u32 s14, s10, s28
	s_addc_u32 s15, s11, 0
	s_mul_i32 s28, s21, 0x1c00000
	s_add_u32 s28, s28, 0x7800000
	s_add_u32 s16, s86, s28
	s_addc_u32 s17, s87, 0
	s_movk_i32 s24, 0x7000
	s_movk_i32 s25, 0x800
	s_mov_b32 s26, 0x43800000
	s_lshr_b32 s22, s20, 4
	s_mul_i32 s22, s22, 0x2493
	s_lshr_b32 s22, s22, 16
	s_mul_i32 s28, s22, 0x70
	s_sub_i32 s23, s20, s28
	s_mov_b32 s29, 1
	s_branch .Lsf8_dec

; __device__ __forceinline__ void transpose_item_f8(const float* W, int N, unsigned char* WT, int ldt, int kind, int off, int item, int lane, float scale) {
;     const int nblk = N >> 6, kb = item / nblk, nb = item - kb * nblk, k0 = 128 * kb + 16 * (lane & 7), n = 64 * nb + 4 * (lane >> 3);
; __device__ __forceinline__ void moe_convert(Frame& F, int lo, int hi, int rank, int nrank) {
;     ...
;     for (int it = lo + rank; it < hi; it += nrank) {
;         int r = it; const float* W; unsigned char* WT; int N, ldt, kind, off; float f8s;
;         if (r < 14336) { const int e = r / 1792; r -= e * 1792; W = F.in[IN_WMG] + (size_t)e * 2048 * DFFE; N = DFFE; WT = F.ws + WS_WGU1 + (size_t)e * 14336 * 2048; ldt = 2048; kind = 1; off = 0; f8s = 32.f; }
;         else if ((r -= 14336) < 14336) { const int e = r / 1792; r -= e * 1792; W = F.in[IN_WMU] + (size_t)e * 2048 * DFFE; N = DFFE; WT = F.ws + WS_WGU1 + (size_t)e * 14336 * 2048; ldt = 2048; kind = 1; off = 128; f8s = 256.f; }
;         else { r -= 14336; const int e = r / 1792; r -= e * 1792; W = F.in[IN_WMD] + (size_t)e * DFFE * 2048; N = 2048; WT = F.ws + WS_WDN1 + (size_t)e * 2048 * DFFE; ldt = DFFE; kind = 0; off = 0; f8s = 64.f; }
;         transpose_item_f8(W, N, WT, ldt, kind, off, r, F.lane, f8s);
.Lsf9_loop:
	ds_read_b32 v9, v8
	s_waitcnt lgkmcnt(0)
	v_readfirstlane_b32 s5, v9
	s_cmp_eq_u32 s5, 10
	s_cbranch_scc1 .Lsf9_done
	ds_add_rtn_u32 v9, v8, v18 offset:4
	s_waitcnt lgkmcnt(0)
	v_readfirstlane_b32 s18, v9
	s_cmp_ge_u32 s18, s40
	s_cbranch_scc1 .Lsf9_done
	s_add_i32 s18, s18, s33
	s_and_b32 s27, s18, 1
	s_lshr_b32 s19, s18, 1
	s_add_i32 s19, s19, 0x5000
	s_cmp_lt_u32 s19, 0x7000
	s_cbranch_scc0 .Lsf9_down
	s_add_i32 s20, s19, 0xffffc800
	s_lshr_b32 s21, s20, 8
	s_mul_i32 s21, s21, 37
	s_lshr_b32 s21, s21, 8
	s_mul_i32 s28, s21, 0x700
	s_sub_i32 s20, s20, s28
	s_mul_i32 s28, s21, 0x3800000
	s_add_u32 s14, s10, s28
	s_addc_u32 s15, s11, 0
	s_mul_i32 s28, s21, 0x1c00000
	s_add_u32 s28, s28, 0x7800000
	s_add_u32 s16, s86, s28
	s_addc_u32 s17, s87, 0
	s_movk_i32 s24, 0x7000
	s_movk_i32 s25, 0x800
	s_mov_b32 s26, 0x43800000
	s_lshr_b32 s22, s20, 4
	s_mul_i32 s22, s22, 0x2493
	s_lshr_b32 s22, s22, 16
	s_mul_i32 s28, s22, 0x70
	s_sub_i32 s23, s20, s28
	s_mov_b32 s29, 1
	s_branch .Lsf9_dec

; __device__ __forceinline__ void transpose_item_f8(const float* W, int N, unsigned char* WT, int ldt, int kind, int off, int item, int lane, float scale) {
;     const int nblk = N >> 6, kb = item / nblk, nb = item - kb * nblk, k0 = 128 * kb + 16 * (lane & 7), n = 64 * nb + 4 * (lane >> 3);
; __device__ __forceinline__ void moe_convert(Frame& F, int lo, int hi, int rank, int nrank) {
;     ...
;     for (int it = lo + rank; it < hi; it += nrank) {
;         int r = it; const float* W; unsigned char* WT; int N, ldt, kind, off; float f8s;
;         if (r < 14336) { const int e = r / 1792; r -= e * 1792; W = F.in[IN_WMG] + (size_t)e * 2048 * DFFE; N = DFFE; WT = F.ws + WS_WGU1 + (size_t)e * 14336 * 2048; ldt = 2048; kind = 1; off = 0; f8s = 32.f; }
;         else if ((r -= 14336) < 14336) { const int e = r / 1792; r -= e * 1792; W = F.in[IN_WMU] + (size_t)e * 2048 * DFFE; N = DFFE; WT = F.ws + WS_WGU1 + (size_t)e * 14336 * 2048; ldt = 2048; kind = 1; off = 128; f8s = 256.f; }
;         else { r -= 14336; const int e = r / 1792; r -= e * 1792; W = F.in[IN_WMD] + (size_t)e * DFFE * 2048; N = 2048; WT = F.ws + WS_WDN1 + (size_t)e * 2048 * DFFE; ldt = DFFE; kind = 0; off = 0; f8s = 64.f; }
;         transpose_item_f8(W, N, WT, ldt, kind, off, r, F.lane, f8s);
.Lsf10_loop:
	ds_read_b32 v9, v8
	s_waitcnt lgkmcnt(0)
	v_readfirstlane_b32 s5, v9
	s_cmp_eq_u32 s5, 11
	s_cbranch_scc1 .Lsf10_done
	ds_add_rtn_u32 v9, v8, v18 offset:4
	s_waitcnt lgkmcnt(0)
	v_readfirstlane_b32 s18, v9
	s_cmp_ge_u32 s18, s40
	s_cbranch_scc1 .Lsf10_done
	s_add_i32 s18, s18, s33
	s_and_b32 s27, s18, 1
	s_lshr_b32 s19, s18, 1
	s_add_i32 s19, s19, 0x5000
	s_cmp_lt_u32 s19, 0x7000
	s_cbranch_scc0 .Lsf10_down
	s_add_i32 s20, s19, 0xffffc800
	s_lshr_b32 s21, s20, 8
	s_mul_i32 s21, s21, 37
	s_lshr_b32 s21, s21, 8
	s_mul_i32 s28, s21, 0x700
	s_sub_i32 s20, s20, s28
	s_mul_i32 s28, s21, 0x3800000
	s_add_u32 s14, s10, s28
	s_addc_u32 s15, s11, 0
	s_mul_i32 s28, s21, 0x1c00000
	s_add_u32 s28, s28, 0x7800000
	s_add_u32 s16, s86, s28
	s_addc_u32 s17, s87, 0
	s_movk_i32 s24, 0x7000
	s_movk_i32 s25, 0x800
	s_mov_b32 s26, 0x43800000
	s_lshr_b32 s22, s20, 4
	s_mul_i32 s22, s22, 0x2493
	s_lshr_b32 s22, s22, 16
	s_mul_i32 s28, s22, 0x70
	s_sub_i32 s23, s20, s28
	s_mov_b32 s29, 1
	s_branch .Lsf10_dec

; __device__ __forceinline__ void transpose_item_f8(const float* W, int N, unsigned char* WT, int ldt, int kind, int off, int item, int lane, float scale) {
;     const int nblk = N >> 6, kb = item / nblk, nb = item - kb * nblk, k0 = 128 * kb + 16 * (lane & 7), n = 64 * nb + 4 * (lane >> 3);
; __device__ __forceinline__ void moe_convert(Frame& F, int lo, int hi, int rank, int nrank) {
;     ...
;     for (int it = lo + rank; it < hi; it += nrank) {
;         int r = it; const float* W; unsigned char* WT; int N, ldt, kind, off; float f8s;
;         if (r < 14336) { const int e = r / 1792; r -= e * 1792; W = F.in[IN_WMG] + (size_t)e * 2048 * DFFE; N = DFFE; WT = F.ws + WS_WGU1 + (size_t)e * 14336 * 2048; ldt = 2048; kind = 1; off = 0; f8s = 32.f; }
;         else if ((r -= 14336) < 14336) { const int e = r / 1792; r -= e * 1792; W = F.in[IN_WMU] + (size_t)e * 2048 * DFFE; N = DFFE; WT = F.ws + WS_WGU1 + (size_t)e * 14336 * 2048; ldt = 2048; kind = 1; off = 128; f8s = 256.f; }
;         else { r -= 14336; const int e = r / 1792; r -= e * 1792; W = F.in[IN_WMD] + (size_t)e * DFFE * 2048; N = 2048; WT = F.ws + WS_WDN1 + (size_t)e * 2048 * DFFE; ldt = DFFE; kind = 0; off = 0; f8s = 64.f; }
;         transpose_item_f8(W, N, WT, ldt, kind, off, r, F.lane, f8s);
.Lsf11_loop:
	ds_read_b32 v9, v8
	s_waitcnt lgkmcnt(0)
	v_readfirstlane_b32 s5, v9
	s_cmp_eq_u32 s5, 12
	s_cbranch_scc1 .Lsf11_done
	ds_add_rtn_u32 v9, v8, v18 offset:4
	s_waitcnt lgkmcnt(0)
	v_readfirstlane_b32 s18, v9
	s_cmp_ge_u32 s18, s40
	s_cbranch_scc1 .Lsf11_done
	s_add_i32 s18, s18, s33
	s_and_b32 s27, s18, 1
	s_lshr_b32 s19, s18, 1
	s_add_i32 s19, s19, 0x5000
	s_cmp_lt_u32 s19, 0x7000
	s_cbranch_scc0 .Lsf11_down
	s_add_i32 s20, s19, 0xffffc800
	s_lshr_b32 s21, s20, 8
	s_mul_i32 s21, s21, 37
	s_lshr_b32 s21, s21, 8
	s_mul_i32 s28, s21, 0x700
	s_sub_i32 s20, s20, s28
	s_mul_i32 s28, s21, 0x3800000
	s_add_u32 s14, s10, s28
	s_addc_u32 s15, s11, 0
	s_mul_i32 s28, s21, 0x1c00000
	s_add_u32 s28, s28, 0x7800000
	s_add_u32 s16, s86, s28
	s_addc_u32 s17, s87, 0
	s_movk_i32 s24, 0x7000
	s_movk_i32 s25, 0x800
	s_mov_b32 s26, 0x43800000
	s_lshr_b32 s22, s20, 4
	s_mul_i32 s22, s22, 0x2493
	s_lshr_b32 s22, s22, 16
	s_mul_i32 s28, s22, 0x70
	s_sub_i32 s23, s20, s28
	s_mov_b32 s29, 1
	s_branch .Lsf11_dec

; __device__ __forceinline__ void transpose_item_f8(const float* W, int N, unsigned char* WT, int ldt, int kind, int off, int item, int lane, float scale) {
;     const int nblk = N >> 6, kb = item / nblk, nb = item - kb * nblk, k0 = 128 * kb + 16 * (lane & 7), n = 64 * nb + 4 * (lane >> 3);
; __device__ __forceinline__ void moe_convert(Frame& F, int lo, int hi, int rank, int nrank) {
;     ...
;     for (int it = lo + rank; it < hi; it += nrank) {
;         int r = it; const float* W; unsigned char* WT; int N, ldt, kind, off; float f8s;
;         if (r < 14336) { const int e = r / 1792; r -= e * 1792; W = F.in[IN_WMG] + (size_t)e * 2048 * DFFE; N = DFFE; WT = F.ws + WS_WGU1 + (size_t)e * 14336 * 2048; ldt = 2048; kind = 1; off = 0; f8s = 32.f; }
;         else if ((r -= 14336) < 14336) { const int e = r / 1792; r -= e * 1792; W = F.in[IN_WMU] + (size_t)e * 2048 * DFFE; N = DFFE; WT = F.ws + WS_WGU1 + (size_t)e * 14336 * 2048; ldt = 2048; kind = 1; off = 128; f8s = 256.f; }
;         else { r -= 14336; const int e = r / 1792; r -= e * 1792; W = F.in[IN_WMD] + (size_t)e * DFFE * 2048; N = 2048; WT = F.ws + WS_WDN1 + (size_t)e * 2048 * DFFE; ldt = DFFE; kind = 0; off = 0; f8s = 64.f; }
;         transpose_item_f8(W, N, WT, ldt, kind, off, r, F.lane, f8s);
.Lsf12_loop:
	ds_read_b32 v9, v8
	s_waitcnt lgkmcnt(0)
	v_readfirstlane_b32 s5, v9
	s_cmp_eq_u32 s5, 13
	s_cbranch_scc1 .Lsf12_done
	ds_add_rtn_u32 v9, v8, v18 offset:4
	s_waitcnt lgkmcnt(0)
	v_readfirstlane_b32 s18, v9
	s_cmp_ge_u32 s18, s40
	s_cbranch_scc1 .Lsf12_done
	s_add_i32 s18, s18, s33
	s_and_b32 s27, s18, 1
	s_lshr_b32 s19, s18, 1
	s_add_i32 s19, s19, 0x5000
	s_cmp_lt_u32 s19, 0x7000
	s_cbranch_scc0 .Lsf12_down
	s_add_i32 s20, s19, 0xffffc800
	s_lshr_b32 s21, s20, 8
	s_mul_i32 s21, s21, 37
	s_lshr_b32 s21, s21, 8
	s_mul_i32 s28, s21, 0x700
	s_sub_i32 s20, s20, s28
	s_mul_i32 s28, s21, 0x3800000
	s_add_u32 s14, s10, s28
	s_addc_u32 s15, s11, 0
	s_mul_i32 s28, s21, 0x1c00000
	s_add_u32 s28, s28, 0x7800000
	s_add_u32 s16, s86, s28
	s_addc_u32 s17, s87, 0
	s_movk_i32 s24, 0x7000
	s_movk_i32 s25, 0x800
	s_mov_b32 s26, 0x43800000
	s_lshr_b32 s22, s20, 4
	s_mul_i32 s22, s22, 0x2493
	s_lshr_b32 s22, s22, 16
	s_mul_i32 s28, s22, 0x70
	s_sub_i32 s23, s20, s28
	s_mov_b32 s29, 1
	s_branch .Lsf12_dec

; __device__ __forceinline__ void transpose_item_f8(const float* W, int N, unsigned char* WT, int ldt, int kind, int off, int item, int lane, float scale) {
;     const int nblk = N >> 6, kb = item / nblk, nb = item - kb * nblk, k0 = 128 * kb + 16 * (lane & 7), n = 64 * nb + 4 * (lane >> 3);
; __device__ __forceinline__ void moe_convert(Frame& F, int lo, int hi, int rank, int nrank) {
;     ...
;     for (int it = lo + rank; it < hi; it += nrank) {
;         int r = it; const float* W; unsigned char* WT; int N, ldt, kind, off; float f8s;
;         if (r < 14336) { const int e = r / 1792; r -= e * 1792; W = F.in[IN_WMG] + (size_t)e * 2048 * DFFE; N = DFFE; WT = F.ws + WS_WGU1 + (size_t)e * 14336 * 2048; ldt = 2048; kind = 1; off = 0; f8s = 32.f; }
;         else if ((r -= 14336) < 14336) { const int e = r / 1792; r -= e * 1792; W = F.in[IN_WMU] + (size_t)e * 2048 * DFFE; N = DFFE; WT = F.ws + WS_WGU1 + (size_t)e * 14336 * 2048; ldt = 2048; kind = 1; off = 128; f8s = 256.f; }
;         else { r -= 14336; const int e = r / 1792; r -= e * 1792; W = F.in[IN_WMD] + (size_t)e * DFFE * 2048; N = 2048; WT = F.ws + WS_WDN1 + (size_t)e * 2048 * DFFE; ldt = DFFE; kind = 0; off = 0; f8s = 64.f; }
;         transpose_item_f8(W, N, WT, ldt, kind, off, r, F.lane, f8s);
.Lsf13_loop:
	ds_read_b32 v9, v8
	s_waitcnt lgkmcnt(0)
	v_readfirstlane_b32 s5, v9
	s_cmp_eq_u32 s5, 14
	s_cbranch_scc1 .Lsf13_done
	ds_add_rtn_u32 v9, v8, v18 offset:4
	s_waitcnt lgkmcnt(0)
	v_readfirstlane_b32 s18, v9
	s_cmp_ge_u32 s18, s40
	s_cbranch_scc1 .Lsf13_done
	s_add_i32 s18, s18, s33
	s_and_b32 s27, s18, 1
	s_lshr_b32 s19, s18, 1
	s_add_i32 s19, s19, 0x5000
	s_cmp_lt_u32 s19, 0x7000
	s_cbranch_scc0 .Lsf13_down
	s_add_i32 s20, s19, 0xffffc800
	s_lshr_b32 s21, s20, 8
	s_mul_i32 s21, s21, 37
	s_lshr_b32 s21, s21, 8
	s_mul_i32 s28, s21, 0x700
	s_sub_i32 s20, s20, s28
	s_mul_i32 s28, s21, 0x3800000
	s_add_u32 s14, s10, s28
	s_addc_u32 s15, s11, 0
	s_mul_i32 s28, s21, 0x1c00000
	s_add_u32 s28, s28, 0x7800000
	s_add_u32 s16, s86, s28
	s_addc_u32 s17, s87, 0
	s_movk_i32 s24, 0x7000
	s_movk_i32 s25, 0x800
	s_mov_b32 s26, 0x43800000
	s_lshr_b32 s22, s20, 4
	s_mul_i32 s22, s22, 0x2493
	s_lshr_b32 s22, s22, 16
	s_mul_i32 s28, s22, 0x70
	s_sub_i32 s23, s20, s28
	s_mov_b32 s29, 1
	s_branch .Lsf13_dec

; __device__ __forceinline__ void moe_convert(Frame& F, int lo, int hi, int rank, int nrank) {
;     ...
;     for (int it = lo + rank; it < hi; it += nrank) {
;         int r = it; const float* W; unsigned char* WT; int N, ldt, kind, off; float f8s;
;         if (r < 14336) { const int e = r / 1792; r -= e * 1792; W = F.in[IN_WMG] + (size_t)e * 2048 * DFFE; N = DFFE; WT = F.ws + WS_WGU1 + (size_t)e * 14336 * 2048; ldt = 2048; kind = 1; off = 0; f8s = 32.f; }
;         else if ((r -= 14336) < 14336) { const int e = r / 1792; r -= e * 1792; W = F.in[IN_WMU] + (size_t)e * 2048 * DFFE; N = DFFE; WT = F.ws + WS_WGU1 + (size_t)e * 14336 * 2048; ldt = 2048; kind = 1; off = 128; f8s = 256.f; }
;         else { r -= 14336; const int e = r / 1792; r -= e * 1792; W = F.in[IN_WMD] + (size_t)e * DFFE * 2048; N = 2048; WT = F.ws + WS_WDN1 + (size_t)e * 2048 * DFFE; ldt = DFFE; kind = 0; off = 0; f8s = 64.f; }
;         transpose_item_f8(W, N, WT, ldt, kind, off, r, F.lane, f8s);
.Lsf14_notw0:
	s_cmp_gt_u32 s4, 7
	s_cbranch_scc1 .Lsf14_skip
	v_mov_b32_e32 v8, 0x20020
	ds_read_b32 v9, v8 offset:4
	v_mbcnt_lo_u32_b32 v2, -1, 0
	v_mbcnt_hi_u32_b32 v2, -1, v2
	v_readlane_b32 s39, v247, 6
	v_readlane_b32 s6, v247, 0
	v_readlane_b32 s7, v247, 1
	s_load_dword s38, s[6:7], 0xe8
	s_movk_i32 s40, 105
	s_and_b32 s41, s39, 7
	s_cmp_ge_u32 s41, 6
	s_cselect_b32 s40, 133, s40
	s_waitcnt lgkmcnt(0)
	v_readfirstlane_b32 s5, v9
	s_cmp_ge_u32 s5, s40
	s_mov_b32 s37, 0
	s_cbranch_scc0 .Lsf14_go
	s_mov_b32 s37, 1
	s_cmpk_eq_u32 s38, 0x100
	s_cbranch_scc1 .Lsf14_skip
.Lsf14_go:
	s_add_i32 s5, s4, -1
	s_lshl_b32 s5, s5, 14
	v_lshl_add_u32 v7, v2, 4, s5
	ds_write_b128 v7, v[160:163] offset:0
	ds_write_b128 v7, v[164:167] offset:1024
	ds_write_b128 v7, v[168:171] offset:2048
	ds_write_b128 v7, v[172:175] offset:3072
	ds_write_b128 v7, v[176:179] offset:4096
	ds_write_b128 v7, v[180:183] offset:5120
	ds_write_b128 v7, v[184:187] offset:6144
	ds_write_b128 v7, v[188:191] offset:7168
	ds_write_b128 v7, v[192:195] offset:8192
	ds_write_b128 v7, v[196:199] offset:9216
	ds_write_b128 v7, v[200:203] offset:10240
	ds_write_b128 v7, v[204:207] offset:11264
	ds_write_b128 v7, v[208:211] offset:12288
	ds_write_b128 v7, v[212:215] offset:13312
	ds_write_b128 v7, v[216:219] offset:14336
	ds_write_b128 v7, v[220:223] offset:15360
	v_readlane_b32 s6, v247, 0
	v_readlane_b32 s7, v247, 1
	s_load_dwordx2 s[10:11], s[6:7], 0xc0
	s_load_dwordx2 s[12:13], s[6:7], 0xc8
	v_mov_b32_e32 v3, 0x43e00000
	v_cmp_eq_u32_e32 vcc, 0, v2
	s_lshr_b32 s42, s39, 3
	s_mul_i32 s42, s42, 896
	s_min_u32 s43, s41, 6
	s_mul_i32 s43, s43, 105
	s_max_u32 s44, s41, 6
	s_sub_u32 s44, s44, 6
	s_mul_i32 s44, s44, 133
	s_add_i32 s33, s42, s43
	s_add_i32 s33, s33, s44
	v_cndmask_b32_e64 v18, 0, 1, vcc
	s_mul_i32 s46, s38, 7
	s_mul_i32 s45, s39, 7
	s_add_i32 s45, s45, s4
	s_add_i32 s45, s45, -1
	s_waitcnt lgkmcnt(0)
.Lsf14_loop:
	s_cmp_eq_u32 s37, 0
	s_cbranch_scc0 .Lsf14_orph
	ds_add_rtn_u32 v9, v8, v18 offset:4
	s_waitcnt lgkmcnt(0)
	v_readfirstlane_b32 s18, v9
	s_cmp_ge_u32 s18, s40
	s_cbranch_scc0 .Lsf14_own
	s_mov_b32 s37, 1
	s_cmpk_eq_u32 s38, 0x100
	s_cbranch_scc1 .Lsf14_done
	s_branch .Lsf14_loop

; __device__ __forceinline__ void moe_convert(Frame& F, int lo, int hi, int rank, int nrank) {
;     ...
;     for (int it = lo + rank; it < hi; it += nrank) {
;         int r = it; const float* W; unsigned char* WT; int N, ldt, kind, off; float f8s;
;         if (r < 14336) { const int e = r / 1792; r -= e * 1792; W = F.in[IN_WMG] + (size_t)e * 2048 * DFFE; N = DFFE; WT = F.ws + WS_WGU1 + (size_t)e * 14336 * 2048; ldt = 2048; kind = 1; off = 0; f8s = 32.f; }
;         else if ((r -= 14336) < 14336) { const int e = r / 1792; r -= e * 1792; W = F.in[IN_WMU] + (size_t)e * 2048 * DFFE; N = DFFE; WT = F.ws + WS_WGU1 + (size_t)e * 14336 * 2048; ldt = 2048; kind = 1; off = 128; f8s = 256.f; }
;         else { r -= 14336; const int e = r / 1792; r -= e * 1792; W = F.in[IN_WMD] + (size_t)e * DFFE * 2048; N = 2048; WT = F.ws + WS_WDN1 + (size_t)e * 2048 * DFFE; ldt = DFFE; kind = 0; off = 0; f8s = 64.f; }
;         transpose_item_f8(W, N, WT, ldt, kind, off, r, F.lane, f8s);
.Lsf14_orph:
	s_mov_b32 s18, s45
	s_cmp_ge_u32 s18, 0x7000
	s_cbranch_scc1 .Lsf14_done
	s_add_i32 s45, s45, s46
	s_mul_hi_u32 s35, s18, 0x492493
	s_mul_i32 s36, s35, 896
	s_sub_i32 s36, s18, s36
	s_cmp_lt_u32 s36, 630
	s_cbranch_scc0 .Lsf14_orphA
	s_mul_hi_u32 s36, s36, 0x2702703
	s_branch .Lsf14_orphO
.Lsf14_orphA:
	s_sub_u32 s36, s36, 630
	s_mul_hi_u32 s36, s36, 0x1ecc07c
	s_add_i32 s36, s36, 6
.Lsf14_orphO:
	s_lshl_b32 s35, s35, 3
	s_add_i32 s35, s35, s36
	s_cmp_lt_u32 s35, s38
	s_cbranch_scc1 .Lsf14_orph
